# PROJ phase start staggered in 8 groups by (bid>>3)&7 x s_sleep 50 to spread epilogue store bursts
# speedup vs baseline: 1.0051x; 1.0051x over previous
.LBB0_269:
	s_cmp_lt_i32 s86, 4
	s_cselect_b64 s[20:21], -1, 0
	s_and_b64 s[0:1], s[20:21], s[0:1]
	s_andn2_b64 vcc, exec, s[0:1]
	v_writelane_b32 v255, s97, 8
	s_cbranch_vccnz .LBB0_801
	s_lshr_b32 s2, s94, 3
	s_and_b32 s2, s2, 7
	s_cmp_eq_u32 s2, 0
	s_cbranch_scc1 .Lstg_done_proj
.Lstg_loop_proj:
	s_sleep 50
	s_sub_u32 s2, s2, 1
	s_cmp_lg_u32 s2, 0
	s_cbranch_scc1 .Lstg_loop_proj
.Lstg_done_proj:
	v_mov_b32_e32 v1, v0
	v_mov_b32_e32 v6, v0
	s_cmpk_lt_i32 s94, 0xb00
	s_cselect_b64 s[0:1], -1, 0
	s_cmpk_gt_i32 s94, 0xaff
	v_readfirstlane_b32 s3, v6
	s_cbranch_scc1 .LBB0_272
	s_ashr_i32 s2, s94, 31
	s_lshr_b32 s2, s2, 29
	s_add_i32 s2, s94, s2
	s_ashr_i32 s4, s2, 3
	s_and_b32 s2, s2, -8
	s_sub_i32 s2, s94, s2
	s_cmp_lt_i32 s2, 0
	s_movk_i32 s5, 0x161
	s_cselect_b32 s5, s5, 0x160
	s_mul_i32 s2, s5, s2
	s_add_i32 s2, s2, s4
	s_mul_hi_i32 s4, s2, 0x2e8ba2e9
	s_lshr_b32 s5, s4, 31
	s_ashr_i32 s4, s4, 6
	s_add_i32 s4, s4, s5
	s_lshl_b32 s5, s4, 3
	s_mulk_i32 s4, 0x160
	s_sub_i32 s2, s2, s4
	s_sext_i32_i16 s4, s2
	s_bfe_u32 s4, s4, 0x3001c
	s_add_i32 s4, s2, s4
	s_sext_i32_i16 s6, s4
	s_and_b32 s4, s4, 0xfff8
	s_sub_i32 s2, s2, s4
	s_sext_i32_i16 s2, s2
	s_add_i32 s2, s5, s2
	s_ashr_i32 s72, s6, 3
